# K1 epilogue: per-wave private reduction slabs (own staging area + 7KB above it) so accumulators are written to LDS without the first epilogue barrier; one barrier removed
# baseline (speedup 1.0000x reference)
.LBB0_8:
	s_or_b64 exec, exec, s[14:15]
	v_lshlrev_b32_e32 v10, 4, v194
	v_readfirstlane_b32 s4, v1
	v_mul_u32_u24_e32 v34, 0x2400, v1
	v_mul_u32_u24_e32 v35, 0x1c00, v1
	s_mov_b32 s7, 0x12000
	v_add_u32_e32 v34, v34, v10
	v_add3_u32 v35, v35, v10, s7
	v_add_u32_e32 v36, 0x400, v34
	v_add_u32_e32 v37, 0x400, v36
	v_add_u32_e32 v38, 0x400, v37
	v_add_u32_e32 v39, 0x400, v38
	v_add_u32_e32 v48, 0x400, v39
	v_add_u32_e32 v49, 0x400, v48
	v_add_u32_e32 v50, 0x400, v49
	v_add_u32_e32 v51, 0x400, v50
	v_add_u32_e32 v52, 0x400, v35
	v_add_u32_e32 v53, 0x400, v52
	v_add_u32_e32 v54, 0x400, v53
	v_add_u32_e32 v55, 0x400, v54
	v_add_u32_e32 v56, 0x400, v55
	v_add_u32_e32 v57, 0x400, v56
	v_lshlrev_b32_e32 v194, 4, v0
	s_mov_b32 s5, 0x1c00
	s_mov_b32 s6, 0x11c00
	s_cmp_eq_u32 s4, 0
	s_cbranch_scc0 .Lep_skip
	s_mov_b32 s5, 0x2400
	s_mov_b32 s6, 0x2000
.Lep_skip:
	v_add_u32_e32 v40, s6, v194
	v_add_u32_e32 v41, s5, v40
	v_add_u32_e32 v42, s5, v41
	v_add_u32_e32 v43, s5, v42
	v_add_u32_e32 v44, s5, v43
	v_add_u32_e32 v45, s5, v44
	v_add_u32_e32 v46, s5, v45
	v_add_u32_e32 v47, s5, v46
	v_add_u32_e32 v66, 0xfc00, v194
	s_waitcnt lgkmcnt(0)
	s_nop 7
	ds_write_b128 v34, v[58:61]
	ds_write_b128 v36, v[62:65]
	ds_write_b128 v37, v[74:77]
	ds_write_b128 v38, v[78:81]
	ds_write_b128 v39, v[82:85]
	ds_write_b128 v48, v[86:89]
	ds_write_b128 v49, v[90:93]
	ds_write_b128 v50, v[94:97]
	ds_write_b128 v51, v[98:101]
	ds_write_b128 v35, v[102:105]
	ds_write_b128 v52, v[106:109]
	ds_write_b128 v53, v[110:113]
	ds_write_b128 v54, v[114:117]
	ds_write_b128 v55, v[118:121]
	ds_write_b128 v56, v[2:5]
	ds_write_b128 v57, v[6:9]
	s_waitcnt lgkmcnt(0)
	s_barrier
	ds_read_b128 v[2:5], v194
	ds_read_b128 v[6:9], v194 offset:9216
	ds_read_b128 v[10:13], v194 offset:18432
	ds_read_b128 v[14:17], v40
	ds_read_b128 v[18:21], v41
	s_nop 0
	s_lshl_b32 s2, s16, 3
	s_or_b32 s2, s2, s17
	s_waitcnt lgkmcnt(3)
	v_pk_add_f32 v[8:9], v[4:5], v[8:9]
	v_pk_add_f32 v[22:23], v[2:3], v[6:7]
	ds_read_b128 v[2:5], v42
	s_waitcnt lgkmcnt(3)
	v_pk_add_f32 v[26:27], v[8:9], v[12:13]
	ds_read_b128 v[6:9], v194 offset:27648
	v_pk_add_f32 v[28:29], v[22:23], v[10:11]
	ds_read_b128 v[10:13], v194 offset:36864
	ds_read_b128 v[22:25], v43
	s_nop 0
	s_ashr_i32 s3, s2, 31
	s_waitcnt lgkmcnt(2)
	v_pk_add_f32 v[26:27], v[26:27], v[8:9]
	v_pk_add_f32 v[28:29], v[28:29], v[6:7]
	ds_read_b128 v[6:9], v194 offset:46080
	s_nop 0
	s_waitcnt lgkmcnt(2)
	v_pk_add_f32 v[30:31], v[26:27], v[12:13]
	v_pk_add_f32 v[32:33], v[28:29], v[10:11]
	ds_read_b128 v[10:13], v194 offset:55296
	s_nop 0
	ds_read_b128 v[26:29], v66
	s_lshl_b64 s[2:3], s[2:3], 14
	s_waitcnt lgkmcnt(2)
	v_pk_add_f32 v[8:9], v[30:31], v[8:9]
	v_pk_add_f32 v[6:7], v[32:33], v[6:7]
	s_add_u32 s2, s12, s2
	s_waitcnt lgkmcnt(1)
	v_pk_add_f32 v[8:9], v[8:9], v[12:13]
	v_pk_add_f32 v[6:7], v[6:7], v[10:11]
	s_addc_u32 s3, s13, s3
	s_waitcnt lgkmcnt(0)
	v_pk_add_f32 v[8:9], v[8:9], v[28:29]
	v_pk_add_f32 v[6:7], v[6:7], v[26:27]
	global_store_dwordx4 v194, v[6:9], s[2:3] sc0 sc1
	s_nop 0
	v_lshl_add_u64 v[26:27], s[2:3], 0, v[194:195]
	v_pk_add_f32 v[6:7], v[16:17], v[20:21]
	v_pk_add_f32 v[8:9], v[14:15], v[18:19]
	v_pk_add_f32 v[6:7], v[6:7], v[4:5]
	v_pk_add_f32 v[8:9], v[8:9], v[2:3]
	ds_read_b128 v[2:5], v44
	s_nop 0
	v_pk_add_f32 v[10:11], v[6:7], v[24:25]
	v_pk_add_f32 v[12:13], v[8:9], v[22:23]
	ds_read_b128 v[6:9], v45
	s_nop 0
	s_waitcnt lgkmcnt(1)
	v_pk_add_f32 v[14:15], v[10:11], v[4:5]
	v_pk_add_f32 v[16:17], v[12:13], v[2:3]
	ds_read_b128 v[2:5], v46
	s_nop 0
	ds_read_b128 v[10:13], v47
	s_waitcnt lgkmcnt(2)
	v_pk_add_f32 v[6:7], v[16:17], v[6:7]
	v_pk_add_f32 v[8:9], v[14:15], v[8:9]
	s_waitcnt lgkmcnt(1)
	v_pk_add_f32 v[2:3], v[6:7], v[2:3]
	v_add_co_u32_e32 v6, vcc, 0x2000, v26
	v_pk_add_f32 v[4:5], v[8:9], v[4:5]
	s_nop 0
	v_addc_co_u32_e32 v7, vcc, 0, v27, vcc
	s_movk_i32 s2, 0x80
	s_waitcnt lgkmcnt(0)
	v_pk_add_f32 v[4:5], v[4:5], v[12:13]
	v_pk_add_f32 v[2:3], v[2:3], v[10:11]
	v_cmp_gt_u32_e32 vcc, s2, v0
	global_store_dwordx4 v[6:7], v[2:5], off sc0 sc1
	s_and_saveexec_b64 s[2:3], vcc
	s_cbranch_execz .LBB0_10
	v_lshlrev_b32_e32 v1, 2, v0
	v_or_b32_e32 v2, 0x20000, v1
	v_add_u32_e32 v3, 0x20200, v1
	v_add_u32_e32 v4, 0x20400, v1
	v_add_u32_e32 v5, 0x20600, v1
	v_or_b32_e32 v6, 0x20800, v1
	v_add_u32_e32 v7, 0x20a00, v1
	v_add_u32_e32 v8, 0x20c00, v1
	v_add_u32_e32 v9, 0x20e00, v1
	ds_read_b32 v2, v2
	ds_read_b32 v3, v3
	ds_read_b32 v4, v4
	ds_read_b32 v5, v5
	ds_read_b32 v6, v6
	ds_read_b32 v7, v7
	ds_read_b32 v8, v8
	ds_read_b32 v9, v9
	s_waitcnt lgkmcnt(7)
	v_add_f32_e32 v2, 0, v2
	s_waitcnt lgkmcnt(6)
	v_add_f32_e32 v2, v2, v3
	s_waitcnt lgkmcnt(5)
	v_add_f32_e32 v2, v2, v4
	s_waitcnt lgkmcnt(4)
	v_add_f32_e32 v2, v2, v5
	s_waitcnt lgkmcnt(3)
	v_add_f32_e32 v2, v2, v6
	s_waitcnt lgkmcnt(2)
	v_add_f32_e32 v2, v2, v7
	s_waitcnt lgkmcnt(1)
	v_add_f32_e32 v2, v2, v8
	s_waitcnt lgkmcnt(0)
	v_add_f32_e32 v2, v2, v9
	v_or_b32_e32 v3, 0x21000, v1
	v_add_u32_e32 v4, 0x21200, v1
	v_add_u32_e32 v5, 0x21400, v1
	v_add_u32_e32 v6, 0x21600, v1
	v_or_b32_e32 v7, 0x21800, v1
	v_add_u32_e32 v8, 0x21a00, v1
	v_add_u32_e32 v9, 0x21c00, v1
	v_add_u32_e32 v1, 0x21e00, v1
	ds_read_b32 v3, v3
	ds_read_b32 v4, v4
	ds_read_b32 v5, v5
	ds_read_b32 v6, v6
	ds_read_b32 v7, v7
	ds_read_b32 v8, v8
	ds_read_b32 v9, v9
	ds_read_b32 v1, v1
	s_waitcnt lgkmcnt(7)
	v_add_f32_e32 v2, v2, v3
	s_waitcnt lgkmcnt(6)
	v_add_f32_e32 v2, v2, v4
	s_waitcnt lgkmcnt(5)
	v_add_f32_e32 v2, v2, v5
	s_waitcnt lgkmcnt(0)
	v_add_f32_e32 v2, v2, v6
	v_add_f32_e32 v2, v2, v7
	s_lshl_b32 s2, s16, 10
	s_lshl_b32 s3, s17, 7
	v_add_f32_e32 v2, v2, v8
	s_or_b32 s2, s2, s3
	v_add_f32_e32 v2, v2, v9
	v_or_b32_e32 v0, s2, v0
	v_add_f32_e32 v2, v2, v1
	v_ashrrev_i32_e32 v1, 31, v0
	v_lshl_add_u64 v[0:1], v[0:1], 2, s[24:25]
	global_store_dword v[0:1], v2, off sc0 sc1
